# baseline (speedup 1.0000x reference)
_Z9ssim_mainPKfS0_S0_Pf:
	v_readfirstlane_b32 s29, v0
	s_load_dwordx4 s[4:7], s[0:1], 0x0
	s_load_dwordx4 s[8:11], s[0:1], 0x10
	s_mov_b32 s51, 0x44800000
	s_mov_b32 s38, 0
	s_mov_b32 s39, -1
	s_lshr_b32 s12, s29, 6
	s_and_b32 s13, s2, 7
	s_lshl_b32 s13, s13, 5
	s_lshr_b32 s14, s2, 3
	s_add_u32 s13, s13, s14
	s_lshr_b32 s14, s13, 3
	s_and_b32 s15, s13, 7
	s_lshl_b32 s16, s14, 20
	s_lshl_b32 s17, s15, 17
	s_add_u32 s16, s16, s17
	s_lshl_b32 s17, s12, 8
	s_add_u32 s16, s16, s17
	s_lshl_b32 s27, s12, 2
	s_add_u32 s27, s27, 0x10000
	v_and_b32_e32 v8, 63, v0
	v_and_b32_e32 v169, 15, v0
	v_bfe_u32 v164, v0, 4, 2
	v_lshrrev_b32_e32 v167, 2, v169
	v_lshlrev_b32_e32 v167, 5, v167
	v_and_b32_e32 v168, 1, v169
	v_lshl_or_b32 v167, v168, 4, v167
	v_bfe_u32 v168, v169, 1, 1
	v_lshl_or_b32 v167, v168, 7, v167
	v_lshl_or_b32 v9, v164, 14, v167
	v_and_b32_e32 v168, 1, v164
	v_lshl_or_b32 v23, v168, 14, v167
	v_lshrrev_b32_e32 v168, 1, v164
	v_lshl_or_b32 v23, v168, 13, v23
	v_add_u32_e32 v237, 0x1000, v9
	v_add_u32_e32 v238, 0x2000, v9
	v_add_u32_e32 v239, 0x3000, v9
	v_add_u32_e32 v240, 0x10000, v9
	v_add_u32_e32 v241, 0x11000, v9
	v_add_u32_e32 v242, 0x12000, v9
	v_add_u32_e32 v243, 0x13000, v9
	s_waitcnt lgkmcnt(0)
	s_load_dwordx8 s[40:47], s[8:9], 0x0
	s_load_dwordx2 s[48:49], s[8:9], 0x20
	s_load_dword s50, s[8:9], 0x28
	s_add_u32 s18, s4, s16
	s_addc_u32 s19, s5, 0
	s_add_u32 s20, s6, s16
	s_addc_u32 s21, s7, 0
	global_load_dwordx4 v[36:39], v9, s[18:19] offset:0 sc1 nt
	global_load_dwordx4 v[40:43], v9, s[18:19] offset:2048 sc1 nt
	global_load_dwordx4 v[68:71], v9, s[20:21] offset:0 sc1 nt
	global_load_dwordx4 v[72:75], v9, s[20:21] offset:2048 sc1 nt
	global_load_dwordx4 v[44:47], v237, s[18:19] offset:0 sc1 nt
	global_load_dwordx4 v[48:51], v237, s[18:19] offset:2048 sc1 nt
	global_load_dwordx4 v[76:79], v237, s[20:21] offset:0 sc1 nt
	global_load_dwordx4 v[80:83], v237, s[20:21] offset:2048 sc1 nt
	global_load_dwordx4 v[52:55], v238, s[18:19] offset:0 sc1 nt
	global_load_dwordx4 v[56:59], v238, s[18:19] offset:2048 sc1 nt
	global_load_dwordx4 v[84:87], v238, s[20:21] offset:0 sc1 nt
	global_load_dwordx4 v[88:91], v238, s[20:21] offset:2048 sc1 nt
	global_load_dwordx4 v[60:63], v239, s[18:19] offset:0 sc1 nt
	global_load_dwordx4 v[64:67], v239, s[18:19] offset:2048 sc1 nt
	global_load_dwordx4 v[92:95], v239, s[20:21] offset:0 sc1 nt
	global_load_dwordx4 v[96:99], v239, s[20:21] offset:2048 sc1 nt
	v_mov_b32_e32 v6, s27
	v_mov_b32_e32 v168, 0
	ds_write_b32 v6, v168 offset:0
	ds_write_b32 v6, v168 offset:32
	ds_write_b32 v6, v168 offset:64
	ds_write_b32 v6, v168 offset:96
	v_lshlrev_b32_e32 v167, 3, v164
	v_xor_b32_e32 v168, 16, v167
	v_sub_u32_e32 v165, v167, v169
	v_sub_u32_e32 v166, v168, v169
	v_add_u32_e32 v172, 0, v165
	v_min_u32_e32 v172, 11, v172
	v_lshlrev_b32_e32 v172, 2, v172
	v_add_u32_e32 v173, 1, v165
	v_min_u32_e32 v173, 11, v173
	v_lshlrev_b32_e32 v173, 2, v173
	v_add_u32_e32 v174, 2, v165
	v_min_u32_e32 v174, 11, v174
	v_lshlrev_b32_e32 v174, 2, v174
	v_add_u32_e32 v175, 3, v165
	v_min_u32_e32 v175, 11, v175
	v_lshlrev_b32_e32 v175, 2, v175
	v_add_u32_e32 v176, 4, v165
	v_min_u32_e32 v176, 11, v176
	v_lshlrev_b32_e32 v176, 2, v176
	v_add_u32_e32 v177, 5, v165
	v_min_u32_e32 v177, 11, v177
	v_lshlrev_b32_e32 v177, 2, v177
	v_add_u32_e32 v178, 6, v165
	v_min_u32_e32 v178, 11, v178
	v_lshlrev_b32_e32 v178, 2, v178
	v_add_u32_e32 v179, 7, v165
	v_min_u32_e32 v179, 11, v179
	v_lshlrev_b32_e32 v179, 2, v179
	v_add_u32_e32 v180, 0, v166
	v_min_u32_e32 v180, 11, v180
	v_lshlrev_b32_e32 v180, 2, v180
	v_add_u32_e32 v181, 1, v166
	v_min_u32_e32 v181, 11, v181
	v_lshlrev_b32_e32 v181, 2, v181
	v_add_u32_e32 v182, 2, v166
	v_min_u32_e32 v182, 11, v182
	v_lshlrev_b32_e32 v182, 2, v182
	v_add_u32_e32 v183, 3, v166
	v_min_u32_e32 v183, 11, v183
	v_lshlrev_b32_e32 v183, 2, v183
	v_add_u32_e32 v184, 4, v166
	v_min_u32_e32 v184, 11, v184
	v_lshlrev_b32_e32 v184, 2, v184
	v_add_u32_e32 v185, 5, v166
	v_min_u32_e32 v185, 11, v185
	v_lshlrev_b32_e32 v185, 2, v185
	v_add_u32_e32 v186, 6, v166
	v_min_u32_e32 v186, 11, v186
	v_lshlrev_b32_e32 v186, 2, v186
	v_add_u32_e32 v187, 7, v166
	v_min_u32_e32 v187, 11, v187
	v_lshlrev_b32_e32 v187, 2, v187
	global_load_dwordx4 v[100:103], v240, s[18:19] offset:0 sc1 nt
	global_load_dwordx4 v[104:107], v240, s[18:19] offset:2048 sc1 nt
	global_load_dwordx4 v[132:135], v240, s[20:21] offset:0 sc1 nt
	global_load_dwordx4 v[136:139], v240, s[20:21] offset:2048 sc1 nt
	global_load_dwordx4 v[108:111], v241, s[18:19] offset:0 sc1 nt
	global_load_dwordx4 v[112:115], v241, s[18:19] offset:2048 sc1 nt
	global_load_dwordx4 v[140:143], v241, s[20:21] offset:0 sc1 nt
	global_load_dwordx4 v[144:147], v241, s[20:21] offset:2048 sc1 nt
	global_load_dwordx4 v[116:119], v242, s[18:19] offset:0 sc1 nt
	global_load_dwordx4 v[120:123], v242, s[18:19] offset:2048 sc1 nt
	global_load_dwordx4 v[148:151], v242, s[20:21] offset:0 sc1 nt
	global_load_dwordx4 v[152:155], v242, s[20:21] offset:2048 sc1 nt
	global_load_dwordx4 v[124:127], v243, s[18:19] offset:0 sc1 nt
	global_load_dwordx4 v[128:131], v243, s[18:19] offset:2048 sc1 nt
	global_load_dwordx4 v[156:159], v243, s[20:21] offset:0 sc1 nt
	global_load_dwordx4 v[160:163], v243, s[20:21] offset:2048 sc1 nt
	s_cmp_eq_u32 s15, 7
	s_cselect_b32 s22, 0, 0x20000
	s_add_u32 s84, s18, s22
	s_addc_u32 s85, s19, 0
	s_add_u32 s86, s18, s22
	s_addc_u32 s87, s19, 0
	s_add_u32 s86, s86, 0x1000
	s_addc_u32 s87, s87, 0
	s_add_u32 s88, s20, s22
	s_addc_u32 s89, s21, 0
	s_add_u32 s90, s20, s22
	s_addc_u32 s91, s21, 0
	s_add_u32 s90, s90, 0x1000
	s_addc_u32 s91, s91, 0
	s_waitcnt lgkmcnt(0)
	v_writelane_b32 v171, s40, 0
	v_writelane_b32 v171, s41, 1
	v_writelane_b32 v171, s42, 2
	v_writelane_b32 v171, s43, 3
	v_writelane_b32 v171, s44, 4
	v_writelane_b32 v171, s45, 5
	v_writelane_b32 v171, s46, 6
	v_writelane_b32 v171, s47, 7
	v_writelane_b32 v171, s48, 8
	v_writelane_b32 v171, s49, 9
	v_writelane_b32 v171, s50, 10
	v_writelane_b32 v171, 0, 11
	v_fma_mixlo_f16 v171, v171, s51, 0
	ds_bpermute_b32 v188, v172, v171
	ds_bpermute_b32 v189, v173, v171
	ds_bpermute_b32 v190, v174, v171
	ds_bpermute_b32 v191, v175, v171
	ds_bpermute_b32 v192, v176, v171
	ds_bpermute_b32 v193, v177, v171
	ds_bpermute_b32 v194, v178, v171
	ds_bpermute_b32 v195, v179, v171
	v_lshlrev_b32_e32 v167, 2, v164
	s_cmp_eq_u32 s12, 0
	s_cselect_b32 s23, 6, 64
	v_add_u32_e32 v168, 0, v167
	v_cmp_gt_u32_e32 vcc, s23, v168
	s_nop 1
	v_cndmask_b32_e64 v15, 0, 1.0, vcc
	v_add_u32_e32 v168, 1, v167
	v_cmp_gt_u32_e32 vcc, s23, v168
	s_nop 1
	v_cndmask_b32_e64 v16, 0, 1.0, vcc
	v_add_u32_e32 v168, 2, v167
	v_cmp_gt_u32_e32 vcc, s23, v168
	s_nop 1
	v_cndmask_b32_e64 v17, 0, 1.0, vcc
	v_add_u32_e32 v168, 3, v167
	v_cmp_gt_u32_e32 vcc, s23, v168
	s_nop 1
	v_cndmask_b32_e64 v18, 0, 1.0, vcc
	v_and_b32_e32 v167, 31, v8
	v_lshlrev_b32_e32 v167, 4, v167
	s_lshl_b32 s24, s12, 11
	s_add_i32 s25, s12, 7
	s_and_b32 s25, s25, 7
	s_lshl_b32 s26, s25, 11
	v_or_b32_e32 v4, s24, v167
	v_or_b32_e32 v5, s26, v167
	s_lshl_b32 s28, s25, 2
	s_add_u32 s28, s28, 0x10000
	v_mov_b32_e32 v7, s28
	v_mov_b32_e32 v19, 0
	v_mov_b32_e32 v20, 0
	v_mov_b32_e32 v21, 0
	v_mov_b32_e32 v22, 0
	s_waitcnt lgkmcnt(7)
	ds_bpermute_b32 v196, v180, v171
	ds_bpermute_b32 v197, v181, v171
	ds_bpermute_b32 v198, v182, v171
	ds_bpermute_b32 v199, v183, v171
	ds_bpermute_b32 v200, v184, v171
	ds_bpermute_b32 v201, v185, v171
	ds_bpermute_b32 v202, v186, v171
	ds_bpermute_b32 v203, v187, v171
	s_waitcnt lgkmcnt(0)
	v_cmp_lt_u32_e64 s[32:33], 31, v8
	v_cmp_gt_u32_e64 s[34:35], 32, v8
	v_pack_b32_f16 v24, v188, v189
	v_pack_b32_f16 v25, v190, v191
	v_pack_b32_f16 v26, v192, v193
	v_pack_b32_f16 v27, v194, v195
	v_pack_b32_f16 v167, v196, v197
	v_cndmask_b32_e64 v28, 0, v167, s[32:33]
	v_cndmask_b32_e64 v32, 0, v167, s[34:35]
	v_pack_b32_f16 v167, v198, v199
	v_cndmask_b32_e64 v29, 0, v167, s[32:33]
	v_cndmask_b32_e64 v33, 0, v167, s[34:35]
	v_pack_b32_f16 v167, v200, v201
	v_cndmask_b32_e64 v30, 0, v167, s[32:33]
	v_cndmask_b32_e64 v34, 0, v167, s[34:35]
	v_pack_b32_f16 v167, v202, v203
	v_cndmask_b32_e64 v31, 0, v167, s[32:33]
	v_cndmask_b32_e64 v35, 0, v167, s[34:35]
	s_waitcnt lgkmcnt(0)
	s_cmp_lt_u32 s12, 4
	s_cbranch_scc1 .Lq_noprio
	s_setprio 1
.Lq_noprio:
	s_waitcnt vmcnt(28)
	v_cvt_pk_f16_f32 v164, v36, v40
	v_cvt_pk_f16_f32 v180, v68, v72
	v_pk_add_f16 v164, v164, -0.5 op_sel_hi:[1,0]
	v_pk_add_f16 v180, v180, -0.5 op_sel_hi:[1,0]
	v_pk_mul_f16 v196, v180, v180
	v_pk_mul_f16 v212, v164, v180
	v_pk_fma_f16 v196, v164, v164, v196
	v_cvt_pk_f16_f32 v168, v37, v41
	v_cvt_pk_f16_f32 v184, v69, v73
	v_pk_add_f16 v168, v168, -0.5 op_sel_hi:[1,0]
	v_pk_add_f16 v184, v184, -0.5 op_sel_hi:[1,0]
	v_pk_mul_f16 v200, v184, v184
	v_pk_mul_f16 v216, v168, v184
	v_pk_fma_f16 v200, v168, v168, v200
	v_cvt_pk_f16_f32 v172, v38, v42
	v_cvt_pk_f16_f32 v188, v70, v74
	v_pk_add_f16 v172, v172, -0.5 op_sel_hi:[1,0]
	v_pk_add_f16 v188, v188, -0.5 op_sel_hi:[1,0]
	v_pk_mul_f16 v204, v188, v188
	v_pk_mul_f16 v220, v172, v188
	v_pk_fma_f16 v204, v172, v172, v204
	v_cvt_pk_f16_f32 v176, v39, v43
	v_cvt_pk_f16_f32 v192, v71, v75
	v_pk_add_f16 v176, v176, -0.5 op_sel_hi:[1,0]
	v_pk_add_f16 v192, v192, -0.5 op_sel_hi:[1,0]
	v_pk_mul_f16 v208, v192, v192
	v_pk_mul_f16 v224, v176, v192
	v_pk_fma_f16 v208, v176, v176, v208
	s_waitcnt vmcnt(24)
	v_cvt_pk_f16_f32 v165, v44, v48
	v_cvt_pk_f16_f32 v181, v76, v80
	v_pk_add_f16 v165, v165, -0.5 op_sel_hi:[1,0]
	v_pk_add_f16 v181, v181, -0.5 op_sel_hi:[1,0]
	v_pk_mul_f16 v197, v181, v181
	v_pk_mul_f16 v213, v165, v181
	v_pk_fma_f16 v197, v165, v165, v197
	v_cvt_pk_f16_f32 v169, v45, v49
	v_cvt_pk_f16_f32 v185, v77, v81
	v_pk_add_f16 v169, v169, -0.5 op_sel_hi:[1,0]
	v_pk_add_f16 v185, v185, -0.5 op_sel_hi:[1,0]
	v_pk_mul_f16 v201, v185, v185
	v_pk_mul_f16 v217, v169, v185
	v_pk_fma_f16 v201, v169, v169, v201
	v_cvt_pk_f16_f32 v173, v46, v50
	v_cvt_pk_f16_f32 v189, v78, v82
	v_pk_add_f16 v173, v173, -0.5 op_sel_hi:[1,0]
	v_pk_add_f16 v189, v189, -0.5 op_sel_hi:[1,0]
	v_pk_mul_f16 v205, v189, v189
	v_pk_mul_f16 v221, v173, v189
	v_pk_fma_f16 v205, v173, v173, v205
	v_cvt_pk_f16_f32 v177, v47, v51
	v_cvt_pk_f16_f32 v193, v79, v83
	v_pk_add_f16 v177, v177, -0.5 op_sel_hi:[1,0]
	v_pk_add_f16 v193, v193, -0.5 op_sel_hi:[1,0]
	v_pk_mul_f16 v209, v193, v193
	v_pk_mul_f16 v225, v177, v193
	v_pk_fma_f16 v209, v177, v177, v209
	s_waitcnt vmcnt(20)
	v_cvt_pk_f16_f32 v166, v52, v56
	v_cvt_pk_f16_f32 v182, v84, v88
	v_pk_add_f16 v166, v166, -0.5 op_sel_hi:[1,0]
	v_pk_add_f16 v182, v182, -0.5 op_sel_hi:[1,0]
	v_pk_mul_f16 v198, v182, v182
	v_pk_mul_f16 v214, v166, v182
	v_pk_fma_f16 v198, v166, v166, v198
	v_cvt_pk_f16_f32 v170, v53, v57
	v_cvt_pk_f16_f32 v186, v85, v89
	v_pk_add_f16 v170, v170, -0.5 op_sel_hi:[1,0]
	v_pk_add_f16 v186, v186, -0.5 op_sel_hi:[1,0]
	v_pk_mul_f16 v202, v186, v186
	v_pk_mul_f16 v218, v170, v186
	v_pk_fma_f16 v202, v170, v170, v202
	v_cvt_pk_f16_f32 v174, v54, v58
	v_cvt_pk_f16_f32 v190, v86, v90
	v_pk_add_f16 v174, v174, -0.5 op_sel_hi:[1,0]
	v_pk_add_f16 v190, v190, -0.5 op_sel_hi:[1,0]
	v_pk_mul_f16 v206, v190, v190
	v_pk_mul_f16 v222, v174, v190
	v_pk_fma_f16 v206, v174, v174, v206
	v_cvt_pk_f16_f32 v178, v55, v59
	v_cvt_pk_f16_f32 v194, v87, v91
	v_pk_add_f16 v178, v178, -0.5 op_sel_hi:[1,0]
	v_pk_add_f16 v194, v194, -0.5 op_sel_hi:[1,0]
	v_pk_mul_f16 v210, v194, v194
	v_pk_mul_f16 v226, v178, v194
	v_pk_fma_f16 v210, v178, v178, v210
	s_waitcnt vmcnt(16)
	v_cvt_pk_f16_f32 v167, v60, v64
	v_cvt_pk_f16_f32 v183, v92, v96
	v_pk_add_f16 v167, v167, -0.5 op_sel_hi:[1,0]
	v_pk_add_f16 v183, v183, -0.5 op_sel_hi:[1,0]
	v_pk_mul_f16 v199, v183, v183
	v_pk_mul_f16 v215, v167, v183
	v_pk_fma_f16 v199, v167, v167, v199
	v_cvt_pk_f16_f32 v171, v61, v65
	v_cvt_pk_f16_f32 v187, v93, v97
	v_pk_add_f16 v171, v171, -0.5 op_sel_hi:[1,0]
	v_pk_add_f16 v187, v187, -0.5 op_sel_hi:[1,0]
	v_pk_mul_f16 v203, v187, v187
	v_pk_mul_f16 v219, v171, v187
	v_pk_fma_f16 v203, v171, v171, v203
	v_cvt_pk_f16_f32 v175, v62, v66
	v_cvt_pk_f16_f32 v191, v94, v98
	v_pk_add_f16 v175, v175, -0.5 op_sel_hi:[1,0]
	v_pk_add_f16 v191, v191, -0.5 op_sel_hi:[1,0]
	v_pk_mul_f16 v207, v191, v191
	v_pk_mul_f16 v223, v175, v191
	v_pk_fma_f16 v207, v175, v175, v207
	v_cvt_pk_f16_f32 v179, v63, v67
	v_cvt_pk_f16_f32 v195, v95, v99
	v_pk_add_f16 v179, v179, -0.5 op_sel_hi:[1,0]
	v_pk_add_f16 v195, v195, -0.5 op_sel_hi:[1,0]
	v_pk_mul_f16 v211, v195, v195
	v_pk_mul_f16 v227, v179, v195
	v_pk_fma_f16 v211, v179, v179, v211
	v_mfma_f32_16x16x32_f16 v[68:71], v[164:167], v[24:27], 0
	v_mfma_f32_16x16x32_f16 v[72:75], v[168:171], v[24:27], 0
	v_mfma_f32_16x16x32_f16 v[76:79], v[172:175], v[24:27], 0
	v_mfma_f32_16x16x32_f16 v[80:83], v[176:179], v[24:27], 0
	v_mfma_f32_16x16x32_f16 v[84:87], v[180:183], v[24:27], 0
	v_mfma_f32_16x16x32_f16 v[88:91], v[184:187], v[24:27], 0
	v_mfma_f32_16x16x32_f16 v[92:95], v[188:191], v[24:27], 0
	v_mfma_f32_16x16x32_f16 v[96:99], v[192:195], v[24:27], 0
	v_mov_b32_e32 v253, 0x44800000
	v_fma_mixlo_f16 v252, s40, v253, 0
	v_cvt_f32_f16_e32 v252, v252
	v_cvt_f64_f32_e32 v[236:237], v252
	v_add_f64 v[236:237], v[236:237], 0
	v_fma_mixlo_f16 v252, s41, v253, 0
	v_cvt_f32_f16_e32 v252, v252
	v_cvt_f64_f32_e32 v[238:239], v252
	v_add_f64 v[236:237], v[236:237], v[238:239]
	v_fma_mixlo_f16 v252, s42, v253, 0
	v_cvt_f32_f16_e32 v252, v252
	v_cvt_f64_f32_e32 v[238:239], v252
	v_add_f64 v[236:237], v[236:237], v[238:239]
	v_fma_mixlo_f16 v252, s43, v253, 0
	v_cvt_f32_f16_e32 v252, v252
	v_cvt_f64_f32_e32 v[238:239], v252
	v_add_f64 v[236:237], v[236:237], v[238:239]
	v_fma_mixlo_f16 v252, s44, v253, 0
	v_cvt_f32_f16_e32 v252, v252
	v_cvt_f64_f32_e32 v[238:239], v252
	v_add_f64 v[236:237], v[236:237], v[238:239]
	v_fma_mixlo_f16 v252, s45, v253, 0
	v_cvt_f32_f16_e32 v252, v252
	v_cvt_f64_f32_e32 v[238:239], v252
	v_add_f64 v[236:237], v[236:237], v[238:239]
	v_fma_mixlo_f16 v252, s46, v253, 0
	v_cvt_f32_f16_e32 v252, v252
	v_cvt_f64_f32_e32 v[238:239], v252
	v_add_f64 v[236:237], v[236:237], v[238:239]
	v_fma_mixlo_f16 v252, s47, v253, 0
	v_cvt_f32_f16_e32 v252, v252
	v_cvt_f64_f32_e32 v[238:239], v252
	v_add_f64 v[236:237], v[236:237], v[238:239]
	v_fma_mixlo_f16 v252, s48, v253, 0
	v_cvt_f32_f16_e32 v252, v252
	v_cvt_f64_f32_e32 v[238:239], v252
	v_add_f64 v[236:237], v[236:237], v[238:239]
	v_fma_mixlo_f16 v252, s49, v253, 0
	v_cvt_f32_f16_e32 v252, v252
	v_cvt_f64_f32_e32 v[238:239], v252
	v_add_f64 v[236:237], v[236:237], v[238:239]
	v_fma_mixlo_f16 v252, s50, v253, 0
	v_cvt_f32_f16_e32 v252, v252
	v_cvt_f64_f32_e32 v[238:239], v252
	v_add_f64 v[236:237], v[236:237], v[238:239]
	v_cvt_pk_f16_f32 v36, v68, v72
	v_cvt_pk_f16_f32 v37, v76, v80
	v_cvt_pk_f16_f32 v38, v69, v73
	v_cvt_pk_f16_f32 v39, v77, v81
	v_cvt_pk_f16_f32 v40, v70, v74
	v_cvt_pk_f16_f32 v41, v78, v82
	v_cvt_pk_f16_f32 v42, v71, v75
	v_cvt_pk_f16_f32 v43, v79, v83
	v_mfma_f32_16x16x32_f16 v[68:71], v[196:199], v[24:27], 0
	v_mfma_f32_16x16x32_f16 v[72:75], v[200:203], v[24:27], 0
	v_mfma_f32_16x16x32_f16 v[76:79], v[204:207], v[24:27], 0
	v_mfma_f32_16x16x32_f16 v[80:83], v[208:211], v[24:27], 0
	v_mul_f64 v[236:237], v[236:237], v[236:237]
	v_mul_f64 v[240:241], v[236:237], 0.5
	v_add_f64 v[242:243], v[240:241], v[240:241]
	s_mov_b32 s36, 0xeb1c432d
	s_mov_b32 s37, 0x3f1a36e2
	v_mul_f64 v[244:245], v[236:237], s[36:37]
	v_mul_f64 v[246:247], v[240:241], v[242:243]
	v_fmac_f64_e32 v[246:247], v[236:237], v[244:245]
	v_add_f64 v[248:249], v[236:237], v[236:237]
	s_mov_b32 s36, 0x487fcb92
	s_mov_b32 s37, 0x3f4d7dbf
	v_mul_f64 v[250:251], v[236:237], s[36:37]
	v_cvt_f32_f64_e32 v0, v[250:251]
	v_mov_b32_e32 v1, v0
	v_mov_b32_e32 v2, v0
	v_mov_b32_e32 v3, v0
	v_cvt_f32_f64_e32 v10, v[242:243]
	v_cvt_f32_f64_e32 v11, v[246:247]
	v_cvt_f32_f64_e32 v12, v[236:237]
	v_cvt_f32_f64_e32 v13, v[248:249]
	v_mul_f64 v[250:251], v[236:237], v[250:251]
	v_cvt_f32_f64_e32 v14, v[250:251]
	v_cvt_pk_f16_f32 v44, v84, v88
	v_cvt_pk_f16_f32 v45, v92, v96
	v_cvt_pk_f16_f32 v46, v85, v89
	v_cvt_pk_f16_f32 v47, v93, v97
	v_cvt_pk_f16_f32 v48, v86, v90
	v_cvt_pk_f16_f32 v49, v94, v98
	v_cvt_pk_f16_f32 v50, v87, v91
	v_cvt_pk_f16_f32 v51, v95, v99
	v_mfma_f32_16x16x32_f16 v[84:87], v[212:215], v[24:27], 0
	v_mfma_f32_16x16x32_f16 v[88:91], v[216:219], v[24:27], 0
	v_mfma_f32_16x16x32_f16 v[92:95], v[220:223], v[24:27], 0
	v_mfma_f32_16x16x32_f16 v[96:99], v[224:227], v[24:27], 0
	v_cvt_pk_f16_f32 v52, v68, v72
	v_cvt_pk_f16_f32 v53, v76, v80
	v_cvt_pk_f16_f32 v54, v69, v73
	v_cvt_pk_f16_f32 v55, v77, v81
	v_cvt_pk_f16_f32 v56, v70, v74
	v_cvt_pk_f16_f32 v57, v78, v82
	v_cvt_pk_f16_f32 v58, v71, v75
	v_cvt_pk_f16_f32 v59, v79, v83
	v_cvt_pk_f16_f32 v60, v84, v88
	v_cvt_pk_f16_f32 v61, v92, v96
	v_cvt_pk_f16_f32 v62, v85, v89
	v_cvt_pk_f16_f32 v63, v93, v97
	v_cvt_pk_f16_f32 v64, v86, v90
	v_cvt_pk_f16_f32 v65, v94, v98
	v_cvt_pk_f16_f32 v66, v87, v91
	v_cvt_pk_f16_f32 v67, v95, v99
	s_mov_b64 exec, s[38:39]
	ds_write_b128 v4, v[40:43] offset:0
	ds_write_b128 v4, v[48:51] offset:512
	ds_write_b128 v4, v[56:59] offset:1024
	ds_write_b128 v4, v[64:67] offset:1536
	s_mov_b64 exec, -1
	v_mfma_f32_16x16x32_f16 v[68:71], v[24:27], v[36:39], 0
	v_mfma_f32_16x16x32_f16 v[72:75], v[24:27], v[44:47], 0
	v_mfma_f32_16x16x32_f16 v[76:79], v[24:27], v[52:55], v[0:3]
	v_mfma_f32_16x16x32_f16 v[80:83], v[24:27], v[60:63], 0
	v_mfma_f32_16x16x32_f16 v[84:87], v[28:31], v[36:39], 0
	v_mfma_f32_16x16x32_f16 v[88:91], v[28:31], v[44:47], 0
	v_mfma_f32_16x16x32_f16 v[92:95], v[28:31], v[52:55], v[0:3]
	v_mfma_f32_16x16x32_f16 v[96:99], v[28:31], v[60:63], 0
	v_mfma_f32_16x16x32_f16 v[84:87], v[32:35], v[40:43], v[84:87]
	v_mfma_f32_16x16x32_f16 v[88:91], v[32:35], v[48:51], v[88:91]
	v_mfma_f32_16x16x32_f16 v[92:95], v[32:35], v[56:59], v[92:95]
	v_mfma_f32_16x16x32_f16 v[96:99], v[32:35], v[64:67], v[96:99]
	s_waitcnt lgkmcnt(0)
	ds_write_b32 v6, v6 offset:0
	ds_read_b32 v9, v7 offset:0
	v_mul_f32_e32 v244, v68, v72
	v_mul_f32_e32 v250, v69, v73
	v_mul_f32_e64 v245, -v72, v72
	v_mul_f32_e64 v251, -v73, v73
	v_add_f32_e32 v246, v68, v72
	v_add_f32_e32 v252, v69, v73
	v_fma_f32 v245, -v68, v68, v245
	v_fma_f32 v251, -v69, v69, v251
	v_fma_f32 v247, v10, v246, v11
	v_fma_f32 v253, v10, v252, v11
	v_fma_f32 v246, v13, v80, v14
	v_fma_f32 v252, v13, v81, v14
	v_fma_f32 v248, v12, v76, v245
	v_fma_f32 v254, v12, v77, v251
	v_fma_f32 v249, 2.0, v244, v247
	v_fma_f32 v255, 2.0, v250, v253
	v_sub_f32_e32 v247, v247, v245
	v_sub_f32_e32 v253, v253, v251
	v_fma_f32 v246, -2.0, v244, v246
	v_fma_f32 v252, -2.0, v250, v252
	v_mul_f32_e32 v247, v247, v248
	v_mul_f32_e32 v253, v253, v254
	v_rcp_f32_e32 v247, v247
	v_rcp_f32_e32 v253, v253
	v_mul_f32_e32 v249, v249, v246
	v_mul_f32_e32 v255, v255, v252
	v_fma_f32 v19, v249, v247, v19
	v_fma_f32 v19, v255, v253, v19
	v_mul_f32_e32 v244, v70, v74
	v_mul_f32_e32 v250, v71, v75
	v_mul_f32_e64 v245, -v74, v74
	v_mul_f32_e64 v251, -v75, v75
	v_add_f32_e32 v246, v70, v74
	v_add_f32_e32 v252, v71, v75
	v_fma_f32 v245, -v70, v70, v245
	v_fma_f32 v251, -v71, v71, v251
	v_fma_f32 v247, v10, v246, v11
	v_fma_f32 v253, v10, v252, v11
	v_fma_f32 v246, v13, v82, v14
	v_fma_f32 v252, v13, v83, v14
	v_fma_f32 v248, v12, v78, v245
	v_fma_f32 v254, v12, v79, v251
	v_fma_f32 v249, 2.0, v244, v247
	v_fma_f32 v255, 2.0, v250, v253
	v_sub_f32_e32 v247, v247, v245
	v_sub_f32_e32 v253, v253, v251
	v_fma_f32 v246, -2.0, v244, v246
	v_fma_f32 v252, -2.0, v250, v252
	v_mul_f32_e32 v247, v247, v248
	v_mul_f32_e32 v253, v253, v254
	v_rcp_f32_e32 v247, v247
	v_rcp_f32_e32 v253, v253
	v_mul_f32_e32 v249, v249, v246
	v_mul_f32_e32 v255, v255, v252
	v_fma_f32 v20, v249, v247, v20
	v_fma_f32 v20, v255, v253, v20
	v_mfma_f32_16x16x32_f16 v[68:71], v[24:27], v[40:43], 0
	v_mfma_f32_16x16x32_f16 v[72:75], v[24:27], v[48:51], 0
	v_mfma_f32_16x16x32_f16 v[76:79], v[24:27], v[56:59], v[0:3]
	v_mfma_f32_16x16x32_f16 v[80:83], v[24:27], v[64:67], 0
	s_barrier
	ds_read_b32 v9, v7 offset:0
	s_waitcnt lgkmcnt(0)
	v_cmp_ne_u32_e32 vcc, 0, v9
	s_cbranch_vccnz .Lq_go_0
